# retention main: prologue de-serialisation - the first V piece's LDS-DMA (buffer 1) is requested together with the ks piece and the q loads, one wait+barrier covers all three
# speedup vs baseline: 1.0046x; 1.0014x over previous
; #define GAS __attribute__((address_space(1)))
; #define RM_WAITBAR() asm volatile("s_waitcnt vmcnt(0) lgkmcnt(0)\n\ts_barrier" ::: "memory")
; #define RM_DMA_KS(buf) do { _Pragma("unroll") for (int i = 0; i < 8; ++i) { const int idx = tid + 512 * i, tok = idx >> 5, c = (idx & 31) ^ (tok & 31); \
;         glds16(PROJ + (size_t)T * 1024 + (hb0 + tok) * 256 + c * 8, (unsigned)__builtin_amdgcn_readfirstlane(ldsb + (buf) * 65536 + i * 8192)); } } while (0)
; #define RM_DMA_V(p, buf) do { _Pragma("unroll") for (int i = 0; i < 8; ++i) { const int idx = tid + 512 * i, tok = (idx >> 2) & 127; \
;         glds16(PROJ + (size_t)2 * T * 1024 + (hb0 + tok) * 512 + (p) * 256 + (idx >> 9) * 32 + (idx & 3) * 8, (unsigned)__builtin_amdgcn_readfirstlane(ldsb + (buf) * 65536 + i * 8192)); } } while (0)
; __device__ __forceinline__ void ret_main_phase(Frame& F, const bf16* PROJ, const bf16* ST, bf16* AO) { LTID();
;     ...
;         int tid = tid_; asm volatile("" : "+v"(tid));
;         const int lane = tid & 63, r32 = lane & 31, hh = lane >> 5, wid = __builtin_amdgcn_readfirstlane(tid >> 6), rg = wid & 3, e2 = wid >> 2;
;         const int voff = (4 * hh + ((lane & 15) >> 2)) * 64 + ((lane >> 4) & 1) * 32 + (lane & 3) * 8;
;         const int U = L + uu, bh = U >> 6, n = U & 63, b = bh >> 2, h = bh & 3;
;         const size_t tokbase = (size_t)b * SEQ + (size_t)n * 128, hb0 = (size_t)bh * SEQ + (size_t)n * 128;
;         const bf16* qrow = PROJ + (hb0 + rg * 32 + r32) * 256 + 8 * hh;
;         const bf16* stb = ST + ((size_t)bh * 64 + n) * 512 * 256;
;         const unsigned ldsb = (unsigned)(uintptr_t)lds + wid * 1024;
;     ...
;         RM_DMA_KS(0);
;         bf16x8 pa[4][2];
;         {
;             bf16x8 qf[16];
; #pragma unroll
;             for (int s = 0; s < 16; ++s) qf[s] = *(const GAS bf16x8*)(qrow + 16 * s);
;             RM_WAITBAR();
;             asm volatile("" :: "v"(qf[0]), "v"(qf[1]), "v"(qf[2]), "v"(qf[3]), "v"(qf[4]), "v"(qf[5]), "v"(qf[6]), "v"(qf[7]), "v"(qf[8]), "v"(qf[9]), "v"(qf[10]), "v"(qf[11]), "v"(qf[12]), "v"(qf[13]), "v"(qf[14]), "v"(qf[15]));
;             RM_DMA_V(0, 1);
.LBB0_365:
	v_mov_b32_e32 v210, v202
	s_nop 0
	v_readfirstlane_b32 s61, v210
	s_ashr_i32 s0, s61, 6
	s_and_b32 s66, s0, 3
	s_lshl_b32 s64, s66, 5
	v_and_b32_e32 v213, 31, v210
	s_add_u32 s34, s24, s30
	s_waitcnt vmcnt(0)
	v_ashrrev_i32_e32 v4, 5, v210
	v_or_b32_e32 v0, s64, v213
	s_addc_u32 s35, s25, s31
	v_ashrrev_i32_e32 v5, 31, v4
	v_lshl_add_u64 v[2:3], s[34:35], 0, v[0:1]
	v_xor_b32_e32 v0, v4, v210
	v_lshl_add_u64 v[4:5], s[34:35], 0, v[4:5]
	v_lshlrev_b64 v[4:5], 9, v[4:5]
	v_lshlrev_b32_e32 v0, 4, v0
	v_lshl_add_u64 v[4:5], s[14:15], 0, v[4:5]
	v_and_b32_e32 v0, 0x1f0, v0
	s_lshl_b32 s0, s0, 10
	v_lshl_add_u64 v[4:5], v[4:5], 0, v[0:1]
	v_add_u32_e32 v209, 0x200, v210
	s_add_i32 s65, s0, 0
	s_mov_b32 m0, s65
	s_nop 0
	global_load_lds_dwordx4 v[4:5], off
	v_ashrrev_i32_e32 v4, 5, v209
	v_ashrrev_i32_e32 v5, 31, v4
	v_xor_b32_e32 v0, v4, v210
	v_lshl_add_u64 v[4:5], s[34:35], 0, v[4:5]
	v_lshlrev_b64 v[4:5], 9, v[4:5]
	v_lshlrev_b32_e32 v0, 4, v0
	v_lshl_add_u64 v[4:5], s[14:15], 0, v[4:5]
	v_and_b32_e32 v0, 0x1f0, v0
	v_lshl_add_u64 v[4:5], v[4:5], 0, v[0:1]
	v_add_u32_e32 v208, 0x400, v210
	s_add_i32 s68, s65, 0x2000
	s_mov_b32 m0, s68
	s_nop 0
	global_load_lds_dwordx4 v[4:5], off
	v_ashrrev_i32_e32 v4, 5, v208
	v_ashrrev_i32_e32 v5, 31, v4
	v_xor_b32_e32 v0, v4, v210
	v_lshl_add_u64 v[4:5], s[34:35], 0, v[4:5]
	v_lshlrev_b64 v[4:5], 9, v[4:5]
	v_lshlrev_b32_e32 v0, 4, v0
	v_lshl_add_u64 v[4:5], s[14:15], 0, v[4:5]
	v_and_b32_e32 v0, 0x1f0, v0
	v_lshl_add_u64 v[4:5], v[4:5], 0, v[0:1]
	v_add_u32_e32 v207, 0x600, v210
	s_add_i32 s69, s65, 0x4000
	s_mov_b32 m0, s69
	s_nop 0
	global_load_lds_dwordx4 v[4:5], off
	v_ashrrev_i32_e32 v4, 5, v207
	v_ashrrev_i32_e32 v5, 31, v4
	v_xor_b32_e32 v0, v4, v210
	v_lshl_add_u64 v[4:5], s[34:35], 0, v[4:5]
	v_lshlrev_b64 v[4:5], 9, v[4:5]
	v_lshlrev_b32_e32 v0, 4, v0
	v_lshl_add_u64 v[4:5], s[14:15], 0, v[4:5]
	v_and_b32_e32 v0, 0x1f0, v0
	v_lshl_add_u64 v[4:5], v[4:5], 0, v[0:1]
	v_add_u32_e32 v206, 0x800, v210
	s_add_i32 s70, s65, 0x6000
	s_mov_b32 m0, s70
	s_nop 0
	global_load_lds_dwordx4 v[4:5], off
	v_ashrrev_i32_e32 v4, 5, v206
	v_ashrrev_i32_e32 v5, 31, v4
	v_xor_b32_e32 v0, v4, v210
	v_lshl_add_u64 v[4:5], s[34:35], 0, v[4:5]
	v_lshlrev_b64 v[4:5], 9, v[4:5]
	v_lshlrev_b32_e32 v0, 4, v0
	v_lshl_add_u64 v[4:5], s[14:15], 0, v[4:5]
	v_and_b32_e32 v0, 0x1f0, v0
	v_lshl_add_u64 v[4:5], v[4:5], 0, v[0:1]
	v_add_u32_e32 v205, 0xa00, v210
	s_add_i32 s46, s65, 0x8000
	s_mov_b32 m0, s46
	s_nop 0
	global_load_lds_dwordx4 v[4:5], off
	v_ashrrev_i32_e32 v4, 5, v205
	v_ashrrev_i32_e32 v5, 31, v4
	v_xor_b32_e32 v0, v4, v210
	v_lshl_add_u64 v[4:5], s[34:35], 0, v[4:5]
	v_lshlrev_b64 v[4:5], 9, v[4:5]
	v_lshlrev_b32_e32 v0, 4, v0
	v_lshl_add_u64 v[4:5], s[14:15], 0, v[4:5]
	v_and_b32_e32 v0, 0x1f0, v0
	v_lshl_add_u64 v[4:5], v[4:5], 0, v[0:1]
	v_add_u32_e32 v204, 0xc00, v210
	s_add_i32 s42, s65, 0xa000
	s_mov_b32 m0, s42
	s_nop 0
	global_load_lds_dwordx4 v[4:5], off
	v_ashrrev_i32_e32 v4, 5, v204
	v_ashrrev_i32_e32 v5, 31, v4
	v_xor_b32_e32 v0, v4, v210
	v_lshl_add_u64 v[4:5], s[34:35], 0, v[4:5]
	v_lshlrev_b64 v[4:5], 9, v[4:5]
	v_lshlrev_b32_e32 v0, 4, v0
	v_lshl_add_u64 v[4:5], s[14:15], 0, v[4:5]
	v_and_b32_e32 v0, 0x1f0, v0
	v_lshl_add_u64 v[4:5], v[4:5], 0, v[0:1]
	v_add_u32_e32 v203, 0xe00, v210
	s_add_i32 s47, s65, 0xc000
	s_mov_b32 m0, s47
	s_nop 0
	global_load_lds_dwordx4 v[4:5], off
	v_ashrrev_i32_e32 v4, 5, v203
	v_ashrrev_i32_e32 v5, 31, v4
	v_xor_b32_e32 v0, v4, v210
	v_lshl_add_u64 v[4:5], s[34:35], 0, v[4:5]
	v_lshlrev_b64 v[4:5], 9, v[4:5]
	v_lshlrev_b32_e32 v0, 4, v0
	v_bfe_u32 v180, v210, 5, 1
	v_lshlrev_b64 v[2:3], 9, v[2:3]
	v_lshl_add_u64 v[4:5], s[14:15], 0, v[4:5]
	v_and_b32_e32 v0, 0x1f0, v0
	v_lshl_add_u64 v[4:5], v[4:5], 0, v[0:1]
	v_lshl_add_u64 v[2:3], s[12:13], 0, v[2:3]
	v_lshlrev_b32_e32 v0, 4, v180
	s_add_i32 s50, s65, 0xe000
	s_mov_b32 m0, s50
	s_nop 0
	global_load_lds_dwordx4 v[4:5], off
	v_lshl_add_u64 v[162:163], v[2:3], 0, v[0:1]
	global_load_dwordx4 v[34:37], v[162:163], off
	global_load_dwordx4 v[122:125], v[162:163], off offset:32
	global_load_dwordx4 v[118:121], v[162:163], off offset:64
	global_load_dwordx4 v[114:117], v[162:163], off offset:96
	global_load_dwordx4 v[110:113], v[162:163], off offset:128
	global_load_dwordx4 v[106:109], v[162:163], off offset:160
	global_load_dwordx4 v[102:105], v[162:163], off offset:192
	global_load_dwordx4 v[98:101], v[162:163], off offset:224
	global_load_dwordx4 v[94:97], v[162:163], off offset:256
	global_load_dwordx4 v[90:93], v[162:163], off offset:288
	global_load_dwordx4 v[82:85], v[162:163], off offset:320
	global_load_dwordx4 v[86:89], v[162:163], off offset:352
	global_load_dwordx4 v[62:65], v[162:163], off offset:384
	global_load_dwordx4 v[58:61], v[162:163], off offset:416
	global_load_dwordx4 v[54:57], v[162:163], off offset:448
	global_load_dwordx4 v[50:53], v[162:163], off offset:480
	v_bfe_u32 v0, v210, 2, 7
	v_lshlrev_b32_e32 v211, 3, v210
	v_lshl_add_u64 v[2:3], s[34:35], 0, v[0:1]
	v_and_b32_e32 v127, 24, v211
	v_lshlrev_b64 v[142:143], 10, v[2:3]
	v_ashrrev_i32_e32 v170, 4, v210
	v_lshl_add_u64 v[2:3], s[18:19], 0, v[142:143]
	v_lshlrev_b32_e32 v0, 1, v127
	v_and_b32_e32 v144, 0xffffffe0, v170
	v_ashrrev_i32_e32 v168, 4, v209
	v_lshl_add_u64 v[2:3], v[2:3], 0, v[0:1]
	v_ashrrev_i32_e32 v145, 31, v144
	v_and_b32_e32 v146, 0xffffffe0, v168
	v_ashrrev_i32_e32 v166, 4, v208
	s_add_i32 s0, s65, 0x10000
	v_lshl_add_u64 v[4:5], v[144:145], 1, v[2:3]
	v_ashrrev_i32_e32 v147, 31, v146
	v_and_b32_e32 v148, 0xffffffe0, v166
	v_ashrrev_i32_e32 v164, 4, v207
	s_mov_b32 m0, s0
	s_nop 0
	global_load_lds_dwordx4 v[4:5], off
; #define LAS __attribute__((address_space(3)))
; __device__ __forceinline__ int crow(int r, int hi) { return (r & 3) + 8 * (r >> 2) + 4 * hi; }
; #define RM_WAITBAR() asm volatile("s_waitcnt vmcnt(0) lgkmcnt(0)\n\ts_barrier" ::: "memory")
; #define RM_DMA_V(p, buf) do { _Pragma("unroll") for (int i = 0; i < 8; ++i) { const int idx = tid + 512 * i, tok = (idx >> 2) & 127; \
;         glds16(PROJ + (size_t)2 * T * 1024 + (hb0 + tok) * 512 + (p) * 256 + (idx >> 9) * 32 + (idx & 3) * 8, (unsigned)__builtin_amdgcn_readfirstlane(ldsb + (buf) * 65536 + i * 8192)); } } while (0)
; __device__ __forceinline__ void ret_main_phase(Frame& F, const bf16* PROJ, const bf16* ST, bf16* AO) { LTID();
;     ...
;             RM_WAITBAR();
;             asm volatile("" :: "v"(qf[0]), "v"(qf[1]), "v"(qf[2]), "v"(qf[3]), "v"(qf[4]), "v"(qf[5]), "v"(qf[6]), "v"(qf[7]), "v"(qf[8]), "v"(qf[9]), "v"(qf[10]), "v"(qf[11]), "v"(qf[12]), "v"(qf[13]), "v"(qf[14]), "v"(qf[15]));
;             RM_DMA_V(0, 1);
; #pragma unroll
;             for (int jb = 0; jb < 4; ++jb) {
;                 f32x16 S = (f32x16){0.f, 0.f, 0.f, 0.f, 0.f, 0.f, 0.f, 0.f, 0.f, 0.f, 0.f, 0.f, 0.f, 0.f, 0.f, 0.f};
;                 if (jb <= rg) {
; #pragma unroll
;                     for (int s = 0; s < 16; ++s) { const bf16x8 a = *(const LAS bf16x8*)(lds + (32 * jb + r32) * 512 + (((2 * s + hh) ^ r32) * 16)); S = __builtin_amdgcn_mfma_f32_32x32x16_bf16(a, qf[s], S, 0, 0, 0); }
;                     if (jb == rg) {
; #pragma unroll
;                         for (int i = 0; i < 16; ++i) if (crow(i, hh) > r32) S[i] = 0.f; }
	v_lshl_add_u64 v[4:5], v[146:147], 1, v[2:3]
	s_add_i32 s43, s65, 0x12000
	s_mov_b32 m0, s43
	s_nop 0
	global_load_lds_dwordx4 v[4:5], off
	v_ashrrev_i32_e32 v149, 31, v148
	v_and_b32_e32 v150, 0xffffffe0, v164
	v_ashrrev_i32_e32 v160, 4, v206
	v_lshl_add_u64 v[4:5], v[148:149], 1, v[2:3]
	s_add_i32 s44, s65, 0x14000
	s_mov_b32 m0, s44
	s_nop 0
	global_load_lds_dwordx4 v[4:5], off
	v_ashrrev_i32_e32 v151, 31, v150
	v_and_b32_e32 v152, 0xffffffe0, v160
	v_ashrrev_i32_e32 v158, 4, v205
	v_lshl_add_u64 v[4:5], v[150:151], 1, v[2:3]
	s_add_i32 s45, s65, 0x16000
	s_mov_b32 m0, s45
	s_nop 0
	global_load_lds_dwordx4 v[4:5], off
	v_ashrrev_i32_e32 v153, 31, v152
	v_and_b32_e32 v154, 0xffffffe0, v158
	v_ashrrev_i32_e32 v128, 4, v204
	v_ashrrev_i32_e32 v126, 4, v203
	v_lshl_add_u64 v[4:5], v[152:153], 1, v[2:3]
	s_add_i32 s51, s65, 0x18000
	s_mov_b32 m0, s51
	s_nop 0
	global_load_lds_dwordx4 v[4:5], off
	v_ashrrev_i32_e32 v155, 31, v154
	v_and_b32_e32 v156, 0xffffffe0, v128
	v_and_b32_e32 v172, 0xffffffe0, v126
	v_lshl_add_u64 v[4:5], v[154:155], 1, v[2:3]
	s_add_i32 s56, s65, 0x1a000
	s_mov_b32 m0, s56
	s_nop 0
	global_load_lds_dwordx4 v[4:5], off
	v_ashrrev_i32_e32 v157, 31, v156
	v_ashrrev_i32_e32 v173, 31, v172
	v_lshrrev_b32_e32 v6, 5, v210
	v_lshl_add_u64 v[4:5], v[156:157], 1, v[2:3]
	s_add_i32 s62, s65, 0x1c000
	s_mov_b32 m0, s62
	s_nop 0
	global_load_lds_dwordx4 v[4:5], off
	v_lshl_add_u64 v[2:3], v[172:173], 1, v[2:3]
	s_add_i32 s63, s65, 0x1e000
	s_mov_b32 m0, s63
	s_nop 0
	global_load_lds_dwordx4 v[2:3], off
	s_waitcnt vmcnt(0) lgkmcnt(0)
	s_barrier
	v_bitop3_b32 v2, v6, v213, 1 bitop3:0x6c
	v_lshl_add_u32 v22, v213, 9, 0
	v_lshlrev_b32_e32 v2, 4, v2
	v_add_u32_e32 v38, v22, v2
	ds_read_b128 v[2:5], v38
	v_bitop3_b32 v18, v180, v213, 2 bitop3:0x36
	v_lshlrev_b32_e32 v18, 4, v18
	v_add_u32_e32 v39, v22, v18
	ds_read_b128 v[18:21], v39
	s_waitcnt lgkmcnt(1)
	v_mfma_f32_32x32x16_bf16 v[2:17], v[2:5], v[34:37], 0
	s_cmp_lg_u32 s66, 0
	s_cselect_b64 s[8:9], -1, 0
	v_lshlrev_b32_e32 v214, 2, v180
	s_and_b64 vcc, exec, s[8:9]
	s_waitcnt lgkmcnt(0)
	v_mfma_f32_32x32x16_bf16 v[2:17], v[18:21], v[122:125], v[2:17]
	v_bitop3_b32 v18, v180, v213, 4 bitop3:0x36
	v_lshlrev_b32_e32 v18, 4, v18
	v_add_u32_e32 v129, v22, v18
	ds_read_b128 v[18:21], v129
	s_waitcnt lgkmcnt(0)
	v_mfma_f32_32x32x16_bf16 v[2:17], v[18:21], v[118:121], v[2:17]
	v_bitop3_b32 v18, v180, v213, 6 bitop3:0x36
	v_lshlrev_b32_e32 v18, 4, v18
	v_add_u32_e32 v130, v22, v18
	ds_read_b128 v[18:21], v130
	s_waitcnt lgkmcnt(0)
	v_mfma_f32_32x32x16_bf16 v[2:17], v[18:21], v[114:117], v[2:17]
	v_bitop3_b32 v18, v180, v213, 8 bitop3:0x36
	v_lshlrev_b32_e32 v18, 4, v18
	v_add_u32_e32 v131, v22, v18
	ds_read_b128 v[18:21], v131
	s_waitcnt lgkmcnt(0)
	v_mfma_f32_32x32x16_bf16 v[2:17], v[18:21], v[110:113], v[2:17]
	v_bitop3_b32 v18, v180, v213, 10 bitop3:0x36
	v_lshlrev_b32_e32 v18, 4, v18
	v_add_u32_e32 v132, v22, v18
	ds_read_b128 v[18:21], v132
	s_waitcnt lgkmcnt(0)
	v_mfma_f32_32x32x16_bf16 v[2:17], v[18:21], v[106:109], v[2:17]
	v_bitop3_b32 v18, v180, v213, 12 bitop3:0x36
	v_lshlrev_b32_e32 v18, 4, v18
	v_add_u32_e32 v133, v22, v18
	ds_read_b128 v[18:21], v133
	s_waitcnt lgkmcnt(0)
	v_mfma_f32_32x32x16_bf16 v[2:17], v[18:21], v[102:105], v[2:17]
	v_bitop3_b32 v18, v180, v213, 14 bitop3:0x36
	v_lshlrev_b32_e32 v18, 4, v18
	v_add_u32_e32 v134, v22, v18
	ds_read_b128 v[18:21], v134
	s_waitcnt lgkmcnt(0)
	v_mfma_f32_32x32x16_bf16 v[2:17], v[18:21], v[98:101], v[2:17]
	v_bitop3_b32 v18, v180, v213, 16 bitop3:0x36
	v_lshlrev_b32_e32 v18, 4, v18
	v_add_u32_e32 v135, v22, v18
	ds_read_b128 v[18:21], v135
	s_waitcnt lgkmcnt(0)
	v_mfma_f32_32x32x16_bf16 v[2:17], v[18:21], v[94:97], v[2:17]
	v_bitop3_b32 v18, v180, v213, 18 bitop3:0x36
	v_lshlrev_b32_e32 v18, 4, v18
	v_add_u32_e32 v136, v22, v18
	ds_read_b128 v[18:21], v136
	s_waitcnt lgkmcnt(0)
	v_mfma_f32_32x32x16_bf16 v[2:17], v[18:21], v[90:93], v[2:17]
	v_bitop3_b32 v18, v180, v213, 20 bitop3:0x36
	v_lshlrev_b32_e32 v18, 4, v18
	v_add_u32_e32 v137, v22, v18
	ds_read_b128 v[18:21], v137
	s_waitcnt lgkmcnt(0)
	v_mfma_f32_32x32x16_bf16 v[2:17], v[18:21], v[82:85], v[2:17]
	v_bitop3_b32 v18, v180, v213, 22 bitop3:0x36
	v_lshlrev_b32_e32 v18, 4, v18
	v_add_u32_e32 v138, v22, v18
	ds_read_b128 v[18:21], v138
	s_waitcnt lgkmcnt(0)
	v_mfma_f32_32x32x16_bf16 v[2:17], v[18:21], v[86:89], v[2:17]
	v_bitop3_b32 v18, v180, v213, 24 bitop3:0x36
	v_lshlrev_b32_e32 v18, 4, v18
	v_add_u32_e32 v139, v22, v18
	ds_read_b128 v[18:21], v139
	s_waitcnt lgkmcnt(0)
	v_mfma_f32_32x32x16_bf16 v[2:17], v[18:21], v[62:65], v[2:17]
	v_bitop3_b32 v18, v180, v213, 26 bitop3:0x36
	v_lshlrev_b32_e32 v18, 4, v18
	v_add_u32_e32 v140, v22, v18
	ds_read_b128 v[18:21], v140
	s_waitcnt lgkmcnt(0)
	v_mfma_f32_32x32x16_bf16 v[2:17], v[18:21], v[58:61], v[2:17]
	v_bitop3_b32 v18, v180, v213, 28 bitop3:0x36
	v_lshlrev_b32_e32 v18, 4, v18
	v_add_u32_e32 v141, v22, v18
	ds_read_b128 v[18:21], v141
	s_waitcnt lgkmcnt(0)
	v_mfma_f32_32x32x16_bf16 v[2:17], v[18:21], v[54:57], v[2:17]
	v_bitop3_b32 v18, v180, v213, 30 bitop3:0x36
	v_lshlrev_b32_e32 v18, 4, v18
	v_add_u32_e32 v159, v22, v18
	ds_read_b128 v[18:21], v159
	s_waitcnt lgkmcnt(0)
	v_mfma_f32_32x32x16_bf16 v[2:17], v[18:21], v[50:53], v[2:17]
	s_cbranch_vccnz .LBB0_367
	v_cmp_lt_u32_e32 vcc, v214, v213
	v_or_b32_e32 v18, 2, v214
	s_nop 8
	v_cndmask_b32_e32 v3, 0, v3, vcc
	v_cmp_le_u32_e32 vcc, v214, v213
	s_nop 1
	v_cndmask_b32_e32 v2, 0, v2, vcc
	v_cmp_le_u32_e32 vcc, v18, v213
	v_or_b32_e32 v18, 3, v214
	s_nop 0
	v_cndmask_b32_e32 v4, 0, v4, vcc
	v_cmp_le_u32_e32 vcc, v18, v213
	v_or_b32_e32 v18, 8, v214
	s_nop 0
	v_cndmask_b32_e32 v5, 0, v5, vcc
	v_cmp_le_u32_e32 vcc, v18, v213
	v_or_b32_e32 v18, 9, v214
	s_nop 0
	v_cndmask_b32_e32 v6, 0, v6, vcc
	v_cmp_le_u32_e32 vcc, v18, v213
	v_or_b32_e32 v18, 10, v214
	s_nop 0
	v_cndmask_b32_e32 v7, 0, v7, vcc
	v_cmp_le_u32_e32 vcc, v18, v213
	v_or_b32_e32 v18, 11, v214
	s_nop 0
	v_cndmask_b32_e32 v8, 0, v8, vcc
	v_cmp_le_u32_e32 vcc, v18, v213
	v_or_b32_e32 v18, 16, v214
	s_nop 0
	v_cndmask_b32_e32 v9, 0, v9, vcc
	v_cmp_le_u32_e32 vcc, v18, v213
	v_or_b32_e32 v18, 17, v214
	s_nop 0
	v_cndmask_b32_e32 v10, 0, v10, vcc
	v_cmp_le_u32_e32 vcc, v18, v213
	v_or_b32_e32 v18, 18, v214
	s_nop 0
	v_cndmask_b32_e32 v11, 0, v11, vcc
	v_cmp_le_u32_e32 vcc, v18, v213
	v_or_b32_e32 v18, 19, v214
	s_nop 0
	v_cndmask_b32_e32 v12, 0, v12, vcc
	v_cmp_le_u32_e32 vcc, v18, v213
	v_or_b32_e32 v18, 24, v214
	s_nop 0
	v_cndmask_b32_e32 v13, 0, v13, vcc
	v_cmp_le_u32_e32 vcc, v18, v213
	v_or_b32_e32 v18, 25, v214
	s_nop 0
	v_cndmask_b32_e32 v14, 0, v14, vcc
	v_cmp_le_u32_e32 vcc, v18, v213
	v_or_b32_e32 v18, 26, v214
	s_nop 0
	v_cndmask_b32_e32 v15, 0, v15, vcc
	v_cmp_le_u32_e32 vcc, v18, v213
	v_or_b32_e32 v18, 27, v214
	s_nop 0
	v_cndmask_b32_e32 v16, 0, v16, vcc
	v_cmp_le_u32_e32 vcc, v18, v213
	s_nop 1
	v_cndmask_b32_e32 v17, 0, v17, vcc
